# attention loop: loop-invariant address math hoisted, V loads via scalar base
# speedup vs baseline: 1.0058x; 1.0022x over previous
.LBB0_438:
	s_lshl_b32 s2, s12, 1
	s_and_b32 s2, s2, 14
	s_ashr_i32 s3, s12, 7
	s_add_i32 s2, s2, s3
	s_ashr_i32 s3, s2, 2
	s_lshl_b32 s22, s3, 8
	s_lshl_b32 s21, s3, 12
	s_lshl_b32 s3, s12, 5
	s_lshl_b32 s2, s2, 7
	v_mov_b32_e32 v205, v3
	v_readlane_b32 s8, v254, 27
	s_and_b32 s3, s3, 0xf00
	s_and_b32 s10, s2, 0x180
	v_mbcnt_lo_u32_b32 v0, -1, 0
	v_mbcnt_hi_u32_b32 v0, -1, v0
	s_add_i32 s13, s22, 0x4000
	v_add_u32_e32 v204, s8, v0
	s_or_b32 s11, s21, s3
	s_lshl_b32 s80, s10, 1
	s_add_u32 s2, s52, s80
	v_lshlrev_b32_e32 v0, 4, v204
	v_add_u32_e32 v6, 0x200, v204
	v_add_u32_e32 v12, 0x400, v204
	v_add_u32_e32 v14, 0x600, v204
	s_addc_u32 s3, s53, 0
	v_and_b32_e32 v2, 0xf0, v0
	v_ashrrev_i32_e32 v36, 4, v204
	v_ashrrev_i32_e32 v38, 4, v6
	v_ashrrev_i32_e32 v40, 4, v12
	v_ashrrev_i32_e32 v42, 4, v14
	v_add_u32_e32 v20, 0x800, v204
	v_add_u32_e32 v22, 0xa00, v204
	v_lshl_add_u64 v[0:1], s[2:3], 0, v[2:3]
	v_add_u32_e32 v4, s11, v36
	s_movk_i32 s18, 0x1400
	v_add_u32_e32 v6, s11, v38
	v_add_u32_e32 v12, s11, v40
	v_add_u32_e32 v14, s11, v42
	v_ashrrev_i32_e32 v44, 4, v20
	v_ashrrev_i32_e32 v46, 4, v22
	v_add_u32_e32 v28, 0xc00, v204
	v_add_u32_e32 v32, 0xe00, v204
	v_mad_i64_i32 v[4:5], s[8:9], v4, s18, v[0:1]
	v_mad_i64_i32 v[8:9], s[8:9], v6, s18, v[0:1]
	v_mad_i64_i32 v[12:13], s[8:9], v12, s18, v[0:1]
	v_mad_i64_i32 v[16:17], s[8:9], v14, s18, v[0:1]
	v_add_u32_e32 v20, s11, v44
	v_add_u32_e32 v22, s11, v46
	v_ashrrev_i32_e32 v47, 4, v28
	v_ashrrev_i32_e32 v48, 4, v32
	global_load_dwordx4 v[4:7], v[4:5], off
	s_nop 0
	global_load_dwordx4 v[8:11], v[8:9], off
	s_nop 0
	global_load_dwordx4 v[12:15], v[12:13], off
	s_nop 0
	global_load_dwordx4 v[16:19], v[16:17], off
	v_mad_i64_i32 v[20:21], s[8:9], v20, s18, v[0:1]
	v_mad_i64_i32 v[24:25], s[8:9], v22, s18, v[0:1]
	v_add_u32_e32 v28, s11, v47
	v_add_u32_e32 v32, s11, v48
	global_load_dwordx4 v[20:23], v[20:21], off
	s_nop 0
	global_load_dwordx4 v[24:27], v[24:25], off
	v_mad_i64_i32 v[28:29], s[8:9], v28, s18, v[0:1]
	v_mad_i64_i32 v[0:1], s[8:9], v32, s18, v[0:1]
	global_load_dwordx4 v[28:31], v[28:29], off
	v_add_u32_e32 v206, 0x11800, v205
	global_load_dwordx4 v[32:35], v[0:1], off
	v_add_u32_e32 v0, v206, v2
	v_mad_u64_u32 v[36:37], s[14:15], v36, s30, v[0:1]
	v_mad_u64_u32 v[38:39], s[14:15], v38, s30, v[0:1]
	v_mad_u64_u32 v[40:41], s[14:15], v40, s30, v[0:1]
	v_mad_u64_u32 v[42:43], s[14:15], v42, s30, v[0:1]
	v_mad_u64_u32 v[44:45], s[14:15], v44, s30, v[0:1]
	v_and_b32_e32 v2, 63, v204
	v_ashrrev_i32_e32 v49, 6, v204
	s_mov_b64 s[24:25], 0x400
	v_readfirstlane_b32 s8, v49
	s_mov_b32 s23, 0
	v_mov_b32_e32 v210, 0
	v_mov_b32_e32 v208, 0xf149f2ca
	v_mov_b32_e32 v209, 0xf149f2ca
	v_mov_b32_e32 v207, 0
	s_waitcnt vmcnt(7)
	ds_write_b128 v36, v[4:7]
	s_waitcnt vmcnt(6)
	ds_write_b128 v38, v[8:11]
	s_waitcnt vmcnt(5)
	ds_write_b128 v40, v[12:15]
	s_waitcnt vmcnt(4)
	ds_write_b128 v42, v[16:19]
	s_waitcnt vmcnt(3)
	ds_write_b128 v44, v[20:23]
	v_mad_u64_u32 v[4:5], s[14:15], v46, s30, v[0:1]
	s_waitcnt vmcnt(2)
	ds_write_b128 v4, v[24:27]
	v_mad_u64_u32 v[4:5], s[14:15], v47, s30, v[0:1]
	v_mad_u64_u32 v[0:1], s[14:15], v48, s30, v[0:1]
	s_waitcnt vmcnt(1)
	ds_write_b128 v4, v[28:31]
	s_waitcnt vmcnt(0)
	ds_write_b128 v0, v[32:35]
	v_or_b32_e32 v4, s13, v2
	v_mov_b64_e32 v[0:1], s[52:53]
	v_mad_i64_i32 v[0:1], s[14:15], v4, s18, v[0:1]
	s_lshl_b32 s14, s8, 3
	s_add_i32 s15, s21, 0xffffff00
	s_cmp_lt_i32 s8, 32
	s_cselect_b32 s9, s13, s15
	s_add_i32 s9, s9, s14
	s_mul_hi_i32 s18, s9, 0x1400
	s_mulk_i32 s9, 0x1400
	s_add_u32 s9, s52, s9
	v_lshlrev_b32_e32 v4, 3, v49
	s_addc_u32 s19, s53, s18
	v_lshl_add_u64 v[0:1], v[0:1], 0, s[80:81]
	v_ashrrev_i32_e32 v5, 31, v4
	s_add_u32 s18, s9, s80
	v_lshl_add_u64 v[0:1], v[4:5], 1, v[0:1]
	s_addc_u32 s19, s19, 0
	v_lshlrev_b32_e32 v2, 2, v2
	global_load_dwordx4 v[176:179], v[0:1], off offset:2048
	global_load_dwordx4 v[180:183], v[0:1], off offset:2176
	v_lshl_add_u64 v[0:1], s[18:19], 0, v[2:3]
	s_mul_i32 s19, s8, 0x880
	v_add_u32_e32 v4, s19, v205
	s_or_b32 s20, s14, 1
	v_readfirstlane_b32 s9, v4
	s_cmpk_lt_i32 s20, 0x100
	s_mov_b32 m0, s9
	s_cselect_b32 s9, s13, s15
	s_add_i32 s9, s9, s20
	s_mul_hi_i32 s18, s9, 0x1400
	s_mulk_i32 s9, 0x1400
	s_add_u32 s9, s52, s9
	s_mulk_i32 s20, 0x110
	s_addc_u32 s18, s53, s18
	v_add_u32_e32 v4, s20, v205
	v_lshl_add_u64 v[0:1], v[0:1], 0, s[24:25]
	s_add_u32 s26, s9, s80
	v_readfirstlane_b32 s9, v4
	global_load_lds_dword v[0:1], off
	s_addc_u32 s27, s18, 0
	s_mov_b32 m0, s9
	s_or_b32 s9, s14, 2
	s_cmpk_lt_i32 s9, 0x100
	s_cselect_b32 s18, s13, s15
	s_add_i32 s9, s18, s9
	s_mul_hi_i32 s18, s9, 0x1400
	s_mulk_i32 s9, 0x1400
	s_add_u32 s9, s52, s9
	s_addc_u32 s18, s53, s18
	v_lshl_add_u64 v[0:1], s[26:27], 0, v[2:3]
	s_add_u32 s26, s9, s80
	s_addc_u32 s27, s18, 0
	s_add_i32 s9, s20, 0x110
	v_add_u32_e32 v4, s9, v205
	v_lshl_add_u64 v[0:1], v[0:1], 0, s[24:25]
	v_readfirstlane_b32 s9, v4
	global_load_lds_dword v[0:1], off
	s_mov_b32 m0, s9
	s_or_b32 s9, s14, 3
	s_cmpk_lt_i32 s9, 0x100
	s_cselect_b32 s18, s13, s15
	s_add_i32 s9, s18, s9
	s_mul_hi_i32 s18, s9, 0x1400
	s_mulk_i32 s9, 0x1400
	s_add_u32 s9, s52, s9
	s_addc_u32 s18, s53, s18
	v_lshl_add_u64 v[0:1], s[26:27], 0, v[2:3]
	s_add_u32 s26, s9, s80
	s_addc_u32 s27, s18, 0
	s_add_i32 s9, s20, 0x220
	v_add_u32_e32 v4, s9, v205
	v_lshl_add_u64 v[0:1], v[0:1], 0, s[24:25]
	v_readfirstlane_b32 s9, v4
	global_load_lds_dword v[0:1], off
	s_mov_b32 m0, s9
	s_or_b32 s9, s14, 4
	s_cmpk_lt_i32 s9, 0x100
	s_cselect_b32 s18, s13, s15
	s_add_i32 s9, s18, s9
	s_mul_hi_i32 s18, s9, 0x1400
	s_mulk_i32 s9, 0x1400
	s_add_u32 s9, s52, s9
	s_addc_u32 s18, s53, s18
	v_lshl_add_u64 v[0:1], s[26:27], 0, v[2:3]
	s_add_u32 s26, s9, s80
	s_addc_u32 s27, s18, 0
	s_add_i32 s9, s20, 0x330
	v_add_u32_e32 v4, s9, v205
	v_lshl_add_u64 v[0:1], v[0:1], 0, s[24:25]
	v_readfirstlane_b32 s9, v4
	global_load_lds_dword v[0:1], off
	s_mov_b32 m0, s9
	s_or_b32 s9, s14, 5
	s_cmpk_lt_i32 s9, 0x100
	s_cselect_b32 s18, s13, s15
	s_add_i32 s9, s18, s9
	s_mul_hi_i32 s18, s9, 0x1400
	s_mulk_i32 s9, 0x1400
	s_add_u32 s9, s52, s9
	s_addc_u32 s18, s53, s18
	v_lshl_add_u64 v[0:1], s[26:27], 0, v[2:3]
	s_add_u32 s26, s9, s80
	s_addc_u32 s27, s18, 0
	s_add_i32 s9, s20, 0x440
	v_add_u32_e32 v4, s9, v205
	v_lshl_add_u64 v[0:1], v[0:1], 0, s[24:25]
	v_readfirstlane_b32 s9, v4
	global_load_lds_dword v[0:1], off
	s_mov_b32 m0, s9
	s_or_b32 s9, s14, 6
	s_cmpk_lt_i32 s9, 0x100
	s_cselect_b32 s18, s13, s15
	s_add_i32 s9, s18, s9
	s_mul_hi_i32 s18, s9, 0x1400
	s_mulk_i32 s9, 0x1400
	s_add_u32 s9, s52, s9
	s_addc_u32 s18, s53, s18
	v_lshl_add_u64 v[0:1], s[26:27], 0, v[2:3]
	s_add_u32 s26, s9, s80
	s_addc_u32 s27, s18, 0
	s_add_i32 s9, s20, 0x550
	v_add_u32_e32 v4, s9, v205
	v_lshl_add_u64 v[0:1], v[0:1], 0, s[24:25]
	v_readfirstlane_b32 s9, v4
	global_load_lds_dword v[0:1], off
	s_mov_b32 m0, s9
	s_or_b32 s9, s14, 7
	s_cmpk_lt_i32 s9, 0x100
	s_cselect_b32 s18, s13, s15
	s_add_i32 s9, s18, s9
	s_mul_hi_i32 s18, s9, 0x1400
	s_mulk_i32 s9, 0x1400
	s_add_u32 s9, s52, s9
	s_addc_u32 s18, s53, s18
	v_lshl_add_u64 v[0:1], s[26:27], 0, v[2:3]
	s_add_u32 s26, s9, s80
	v_lshl_add_u64 v[0:1], v[0:1], 0, s[24:25]
	s_addc_u32 s27, s18, 0
	s_add_i32 s9, s20, 0x660
	global_load_lds_dword v[0:1], off
	v_lshl_add_u64 v[0:1], s[26:27], 0, v[2:3]
	v_add_u32_e32 v2, s9, v205
	v_lshl_add_u64 v[0:1], v[0:1], 0, s[24:25]
	v_readfirstlane_b32 s9, v2
	s_mov_b32 m0, s9
	s_movk_i32 s9, 0x480
	global_load_lds_dword v[0:1], off
	v_bfe_u32 v0, v204, 2, 2
	v_and_b32_e32 v1, 12, v204
	v_cmp_ne_u32_e32 vcc, 2, v0
	v_mov_b32_e32 v14, v3
	v_mov_b32_e32 v15, v3
	v_cndmask_b32_e32 v1, 4, v1, vcc
	v_cmp_ne_u32_e32 vcc, 1, v0
	v_mov_b32_e32 v2, v3
	v_mov_b32_e32 v4, v3
	v_cndmask_b32_e32 v0, 8, v1, vcc
	v_and_or_b32 v0, v204, 51, v0
	v_mul_lo_u32 v1, v49, s9
	v_lshlrev_b32_e32 v0, 1, v0
	v_add3_u32 v0, v205, v1, v0
	s_waitcnt vmcnt(0)
	ds_write_b16 v0, v176 offset:34816
	ds_write_b16_d16_hi v0, v176 offset:34960
	ds_write_b16 v0, v177 offset:35104
	ds_write_b16_d16_hi v0, v177 offset:35248
	ds_write_b16 v0, v178 offset:35392
	ds_write_b16_d16_hi v0, v178 offset:35536
	ds_write_b16 v0, v179 offset:35680
	ds_write_b16_d16_hi v0, v179 offset:35824
	ds_write_b16 v0, v180 offset:44032
	ds_write_b16_d16_hi v0, v180 offset:44176
	ds_write_b16 v0, v181 offset:44320
	ds_write_b16_d16_hi v0, v181 offset:44464
	ds_write_b16 v0, v182 offset:44608
	ds_write_b16_d16_hi v0, v182 offset:44752
	ds_write_b16 v0, v183 offset:44896
	ds_write_b16_d16_hi v0, v183 offset:45040
	v_mov_b32_e32 v0, v3
	v_mov_b32_e32 v1, v3
	v_mov_b32_e32 v5, v3
	v_mov_b32_e32 v6, v3
	v_mov_b32_e32 v7, v3
	v_mov_b32_e32 v8, v3
	v_mov_b32_e32 v9, v3
	v_mov_b32_e32 v10, v3
	v_mov_b32_e32 v11, v3
	v_mov_b32_e32 v12, v3
	v_mov_b32_e32 v13, v3
	v_mov_b64_e32 v[30:31], v[14:15]
	v_mov_b64_e32 v[62:63], v[14:15]
	v_mov_b64_e32 v[94:95], v[14:15]
	v_mov_b64_e32 v[126:127], v[14:15]
	v_mov_b64_e32 v[46:47], v[14:15]
	v_mov_b64_e32 v[78:79], v[14:15]
	v_mov_b64_e32 v[110:111], v[14:15]
	v_mov_b64_e32 v[142:143], v[14:15]
	s_lshl_b32 s18, s8, 5
	s_addk_i32 s21, 0xff40
	s_addk_i32 s22, 0x4040
	v_mov_b64_e32 v[28:29], v[12:13]
	v_mov_b64_e32 v[26:27], v[10:11]
	v_mov_b64_e32 v[24:25], v[8:9]
	v_mov_b64_e32 v[22:23], v[6:7]
	v_mov_b64_e32 v[20:21], v[4:5]
	v_mov_b64_e32 v[18:19], v[2:3]
	v_mov_b64_e32 v[16:17], v[0:1]
	v_mov_b64_e32 v[60:61], v[12:13]
	v_mov_b64_e32 v[58:59], v[10:11]
	v_mov_b64_e32 v[56:57], v[8:9]
	v_mov_b64_e32 v[54:55], v[6:7]
	v_mov_b64_e32 v[52:53], v[4:5]
	v_mov_b64_e32 v[50:51], v[2:3]
	v_mov_b64_e32 v[48:49], v[0:1]
	v_mov_b64_e32 v[92:93], v[12:13]
	v_mov_b64_e32 v[90:91], v[10:11]
	v_mov_b64_e32 v[88:89], v[8:9]
	v_mov_b64_e32 v[86:87], v[6:7]
	v_mov_b64_e32 v[84:85], v[4:5]
	v_mov_b64_e32 v[82:83], v[2:3]
	v_mov_b64_e32 v[80:81], v[0:1]
	v_mov_b64_e32 v[124:125], v[12:13]
	v_mov_b64_e32 v[122:123], v[10:11]
	v_mov_b64_e32 v[120:121], v[8:9]
	v_mov_b64_e32 v[118:119], v[6:7]
	v_mov_b64_e32 v[116:117], v[4:5]
	v_mov_b64_e32 v[114:115], v[2:3]
	v_mov_b64_e32 v[112:113], v[0:1]
	v_mov_b64_e32 v[44:45], v[12:13]
	v_mov_b64_e32 v[42:43], v[10:11]
	v_mov_b64_e32 v[40:41], v[8:9]
	v_mov_b64_e32 v[38:39], v[6:7]
	v_mov_b64_e32 v[36:37], v[4:5]
	v_mov_b64_e32 v[34:35], v[2:3]
	v_mov_b64_e32 v[32:33], v[0:1]
	v_mov_b64_e32 v[76:77], v[12:13]
	v_mov_b64_e32 v[74:75], v[10:11]
	v_mov_b64_e32 v[72:73], v[8:9]
	v_mov_b64_e32 v[70:71], v[6:7]
	v_mov_b64_e32 v[68:69], v[4:5]
	v_mov_b64_e32 v[66:67], v[2:3]
	v_mov_b64_e32 v[64:65], v[0:1]
	v_mov_b64_e32 v[108:109], v[12:13]
	v_mov_b64_e32 v[106:107], v[10:11]
	v_mov_b64_e32 v[104:105], v[8:9]
	v_mov_b64_e32 v[102:103], v[6:7]
	v_mov_b64_e32 v[100:101], v[4:5]
	v_mov_b64_e32 v[98:99], v[2:3]
	v_mov_b64_e32 v[96:97], v[0:1]
	v_mov_b64_e32 v[140:141], v[12:13]
	v_mov_b64_e32 v[138:139], v[10:11]
	v_mov_b64_e32 v[136:137], v[8:9]
	v_mov_b64_e32 v[134:135], v[6:7]
	v_mov_b64_e32 v[132:133], v[4:5]
	v_mov_b64_e32 v[130:131], v[2:3]
	v_mov_b64_e32 v[128:129], v[0:1]
	s_mov_b32 s26, 0
	s_waitcnt lgkmcnt(0)
	s_barrier
	v_and_b32_e32 v2, 31, v204
	v_bfe_u32 v15, v204, 5, 1
	v_lshlrev_b32_e32 v15, 4, v15
	v_or_b32_e32 v13, s18, v2
	v_mul_u32_u24_e32 v1, 0x90, v2
	v_mad_u32_u24 v0, v2, s30, v15
	v_mul_lo_u32 v13, v13, s30
	v_add_u32_e32 v0, v0, v205
	v_add3_u32 v1, v1, v15, v205
	v_add3_u32 v13, v206, v13, v15
	v_bfe_u32 v15, v204, 2, 2
	v_and_b32_e32 v2, 12, v204
	v_cmp_ne_u32_e32 vcc, 2, v15
	s_movk_i32 s8, 0x480
	v_ashrrev_i32_e32 v211, 6, v204
	v_cndmask_b32_e32 v2, 4, v2, vcc
	v_cmp_ne_u32_e32 vcc, 1, v15
	v_mul_lo_u32 v211, v211, s8
	s_nop 0
	v_cndmask_b32_e32 v15, 8, v2, vcc
	v_and_or_b32 v2, v204, 51, v15
	v_lshlrev_b32_e32 v2, 1, v2
	v_add3_u32 v2, v205, v211, v2
.LBB0_439:
	s_add_i32 s25, s26, 1
	s_and_b32 s27, s26, 1
	s_mul_i32 s24, s27, 0x4400
	s_mul_i32 s31, s27, 0x4800
	v_add_u32_e32 v12, s24, v0
	v_add_u32_e32 v14, s31, v1
	ds_read_b128 v[228:231], v12 offset:0
	ds_read_b128 v[232:235], v12 offset:32
	ds_read_b128 v[236:239], v12 offset:64
	ds_read_b128 v[240:243], v12 offset:96
	ds_read_b128 v[244:247], v13 offset:0
	ds_read_b128 v[248:251], v13 offset:32
	ds_read_b128 v[4:7], v13 offset:64
	ds_read_b128 v[8:11], v13 offset:96
	ds_read_b128 v[184:187], v14 offset:34816
	ds_read_b128 v[188:191], v14 offset:39424
	ds_read_b128 v[192:195], v14 offset:44032
	ds_read_b128 v[196:199], v14 offset:48640
	ds_read_b128 v[200:203], v14 offset:34848
	ds_read_b128 v[212:215], v14 offset:39456
	ds_read_b128 v[216:219], v14 offset:44064
	s_cmpk_gt_u32 s26, 0x42
	s_cbranch_scc1 .Lat_noload
	s_cmp_lt_u32 s26, 3
	s_cselect_b32 s24, s22, s21
	s_cselect_b32 s31, s13, s15
	s_add_i32 s24, s24, s23
	v_and_b32_e32 v15, 63, v204
	v_ashrrev_i32_e32 v227, 6, v204
	v_add_u32_e32 v211, s24, v15
	v_lshlrev_b32_e32 v227, 4, v227
	s_add_i32 s31, s31, s14
	v_mul_u32_u24_e32 v211, 0x1400, v211
	s_add_i32 s31, s31, s23
	s_add_i32 s31, s31, 64
	v_add_u32_e32 v211, v211, v227
	s_mul_hi_i32 s37, s31, 0x1400
	s_mul_i32 s36, s31, 0x1400
	v_lshlrev_b32_e32 v15, 2, v15
	global_load_dwordx4 v[176:179], v211, s[2:3] offset:2048
	global_load_dwordx4 v[180:183], v211, s[2:3] offset:2176
	s_add_u32 s36, s2, s36
	s_addc_u32 s37, s3, s37
	v_readfirstlane_b32 s38, v205
	s_xor_b32 s39, s27, 1
	v_add_u32_e32 v15, 0x400, v15
	s_mul_i32 s39, s39, 0x4400
	s_add_i32 s38, s38, s19
	s_add_i32 s38, s38, s39
	s_add_i32 m0, s38, 0
	s_nop 0
	global_load_lds_dword v15, s[36:37]
	s_add_u32 s36, s36, 0x1400
	s_addc_u32 s37, s37, 0
	s_add_i32 m0, s38, 272
	s_nop 0
	global_load_lds_dword v15, s[36:37]
	s_add_u32 s36, s36, 0x1400
	s_addc_u32 s37, s37, 0
	s_add_i32 m0, s38, 544
	s_nop 0
	global_load_lds_dword v15, s[36:37]
	s_add_u32 s36, s36, 0x1400
	s_addc_u32 s37, s37, 0
	s_add_i32 m0, s38, 816
	s_nop 0
	global_load_lds_dword v15, s[36:37]
	s_add_u32 s36, s36, 0x1400
	s_addc_u32 s37, s37, 0
	s_add_i32 m0, s38, 1088
	s_nop 0
	global_load_lds_dword v15, s[36:37]
	s_add_u32 s36, s36, 0x1400
	s_addc_u32 s37, s37, 0
	s_add_i32 m0, s38, 1360
	s_nop 0
	global_load_lds_dword v15, s[36:37]
	s_add_u32 s36, s36, 0x1400
	s_addc_u32 s37, s37, 0
	s_add_i32 m0, s38, 1632
	s_nop 0
	global_load_lds_dword v15, s[36:37]
	s_add_u32 s36, s36, 0x1400
	s_addc_u32 s37, s37, 0
	s_add_i32 m0, s38, 1904
	s_nop 0
	global_load_lds_dword v15, s[36:37]

.Lat_back0_s1:
	v_mfma_f32_32x32x16_bf16 v[48:63], v[192:195], v[160:163], v[48:63]
	v_sub_f32_e32 v144, v144, v209
	v_sub_f32_e32 v145, v145, v209
	v_sub_f32_e32 v146, v146, v209
	v_sub_f32_e32 v147, v147, v209
	v_exp_f32_e32 v144, v144
	v_exp_f32_e32 v145, v145
	v_mfma_f32_32x32x16_bf16 v[16:31], v[196:199], v[160:163], v[16:31]
	v_exp_f32_e32 v146, v146
	v_exp_f32_e32 v147, v147
	v_sub_f32_e32 v148, v148, v209
	v_sub_f32_e32 v149, v149, v209
	v_sub_f32_e32 v150, v150, v209
	v_sub_f32_e32 v151, v151, v209
	v_mfma_f32_32x32x16_bf16 v[112:127], v[200:203], v[164:167], v[112:127]
	v_exp_f32_e32 v148, v148
	v_exp_f32_e32 v149, v149
	v_exp_f32_e32 v150, v150
	v_mfma_f32_32x32x16_bf16 v[80:95], v[212:215], v[164:167], v[80:95]
	v_exp_f32_e32 v151, v151
	v_sub_f32_e32 v152, v152, v209
	v_sub_f32_e32 v153, v153, v209
	v_sub_f32_e32 v154, v154, v209
	v_sub_f32_e32 v155, v155, v209
	v_exp_f32_e32 v152, v152
	v_mfma_f32_32x32x16_bf16 v[48:63], v[216:219], v[164:167], v[48:63]
	v_exp_f32_e32 v153, v153
	v_exp_f32_e32 v154, v154
	v_exp_f32_e32 v155, v155
	v_mfma_f32_32x32x16_bf16 v[16:31], v[220:223], v[164:167], v[16:31]
	v_sub_f32_e32 v156, v156, v209
	v_sub_f32_e32 v157, v157, v209
	v_sub_f32_e32 v158, v158, v209
	v_sub_f32_e32 v159, v159, v209
	v_exp_f32_e32 v156, v156
	v_exp_f32_e32 v157, v157
	ds_read_b128 v[184:187], v14 offset:34880
	ds_read_b128 v[188:191], v14 offset:39488
	ds_read_b128 v[192:195], v14 offset:44096
	ds_read_b128 v[196:199], v14 offset:48704
	ds_read_b128 v[200:203], v14 offset:34912
	ds_read_b128 v[212:215], v14 offset:39520
	ds_read_b128 v[216:219], v14 offset:44128
	s_waitcnt lgkmcnt(7)
	ds_read_b128 v[220:223], v14 offset:48736
	v_mfma_f32_32x32x16_bf16 v[160:175], v[228:231], v[244:247], 0
	v_exp_f32_e32 v158, v158
	v_exp_f32_e32 v159, v159
	v_add_f32_e32 v15, v144, v145
	v_add_f32_e32 v211, v146, v147
	v_add_f32_e32 v15, v15, v211
	v_mfma_f32_32x32x16_bf16 v[160:175], v[232:235], v[248:251], v[160:175]
	v_add_f32_e32 v211, v148, v149
	v_add_f32_e32 v224, v150, v151
	v_add_f32_e32 v211, v211, v224
	v_add_f32_e32 v224, v152, v153
	v_add_f32_e32 v225, v154, v155
	v_add_f32_e32 v224, v224, v225
	v_add_f32_e32 v225, v156, v157
	v_add_f32_e32 v227, v158, v159
	v_add_f32_e32 v225, v225, v227
	v_add_f32_e32 v15, v15, v211
	v_add_f32_e32 v224, v224, v225
	v_mfma_f32_32x32x16_bf16 v[160:175], v[236:239], v[4:7], v[160:175]
	v_add_f32_e32 v15, v15, v224
	v_add_f32_e32 v210, v210, v15
	v_cvt_pk_bf16_f32 v144, v144, v145
	v_cvt_pk_bf16_f32 v145, v146, v147
	v_cvt_pk_bf16_f32 v146, v148, v149
	v_cvt_pk_bf16_f32 v147, v150, v151
	v_cvt_pk_bf16_f32 v148, v152, v153
	v_cvt_pk_bf16_f32 v149, v154, v155
	v_cvt_pk_bf16_f32 v150, v156, v157
	v_cvt_pk_bf16_f32 v151, v158, v159
	v_mfma_f32_32x32x16_bf16 v[160:175], v[240:243], v[8:11], v[160:175]
	s_waitcnt lgkmcnt(0)
	s_nop 0
	v_mfma_f32_32x32x16_bf16 v[128:143], v[184:187], v[144:147], v[128:143]
	s_nop 11
	v_max3_f32 v15, v160, v161, v162
	v_max3_f32 v211, v163, v164, v165
	v_max3_f32 v224, v166, v167, v168
	v_max3_f32 v225, v169, v170, v171
	v_max3_f32 v227, v172, v173, v174
	v_max3_f32 v15, v15, v211, v175
	v_max3_f32 v224, v224, v225, v227
	v_max_f32_e32 v15, v15, v224
	v_mov_b32_e32 v211, v15
	v_add_f32_e32 v225, 0x41000000, v208
	s_nop 1
	v_permlane32_swap_b32_e32 v15, v211
	v_max_f32_e32 v15, v15, v211
	v_cmp_gt_f32_e32 vcc, v15, v225
	s_cbranch_vccnz .Lat_slow1_s1
.Lat_back1_s1:
	v_sub_f32_e32 v160, v160, v208
	v_sub_f32_e32 v161, v161, v208
	v_mfma_f32_32x32x16_bf16 v[96:111], v[188:191], v[144:147], v[96:111]
	v_sub_f32_e32 v162, v162, v208
	v_sub_f32_e32 v163, v163, v208
	v_exp_f32_e32 v160, v160
	v_exp_f32_e32 v161, v161
	v_exp_f32_e32 v162, v162
	v_exp_f32_e32 v163, v163
	v_mfma_f32_32x32x16_bf16 v[64:79], v[192:195], v[144:147], v[64:79]
	v_sub_f32_e32 v164, v164, v208
	v_sub_f32_e32 v165, v165, v208
	v_sub_f32_e32 v166, v166, v208
	v_sub_f32_e32 v167, v167, v208
	v_exp_f32_e32 v164, v164
	v_exp_f32_e32 v165, v165
	v_exp_f32_e32 v166, v166
	v_mfma_f32_32x32x16_bf16 v[32:47], v[196:199], v[144:147], v[32:47]
	v_exp_f32_e32 v167, v167
	v_sub_f32_e32 v168, v168, v208
	v_sub_f32_e32 v169, v169, v208
	v_sub_f32_e32 v170, v170, v208
	v_sub_f32_e32 v171, v171, v208
	v_exp_f32_e32 v168, v168
	v_exp_f32_e32 v169, v169
	v_exp_f32_e32 v170, v170
	v_mfma_f32_32x32x16_bf16 v[128:143], v[200:203], v[148:151], v[128:143]
	v_exp_f32_e32 v171, v171
	v_sub_f32_e32 v172, v172, v208
	v_sub_f32_e32 v173, v173, v208
	v_sub_f32_e32 v174, v174, v208
	v_sub_f32_e32 v175, v175, v208
	v_exp_f32_e32 v172, v172
	v_exp_f32_e32 v173, v173
	v_mfma_f32_32x32x16_bf16 v[96:111], v[212:215], v[148:151], v[96:111]
	v_exp_f32_e32 v174, v174
	v_exp_f32_e32 v175, v175
	v_add_f32_e32 v15, v160, v161
	v_add_f32_e32 v211, v162, v163
	v_add_f32_e32 v15, v15, v211
	v_add_f32_e32 v211, v164, v165
	v_add_f32_e32 v224, v166, v167
	v_add_f32_e32 v211, v211, v224
	v_add_f32_e32 v224, v168, v169
	v_mfma_f32_32x32x16_bf16 v[64:79], v[216:219], v[148:151], v[64:79]
	v_add_f32_e32 v225, v170, v171
	v_add_f32_e32 v224, v224, v225
	v_add_f32_e32 v225, v172, v173
	v_add_f32_e32 v227, v174, v175
	v_add_f32_e32 v225, v225, v227
	v_add_f32_e32 v15, v15, v211
	v_add_f32_e32 v224, v224, v225
	v_add_f32_e32 v15, v15, v224
	v_add_f32_e32 v207, v207, v15
	v_cvt_pk_bf16_f32 v160, v160, v161
	v_cvt_pk_bf16_f32 v161, v162, v163
	v_cvt_pk_bf16_f32 v162, v164, v165
	v_cvt_pk_bf16_f32 v163, v166, v167
	v_cvt_pk_bf16_f32 v164, v168, v169
	v_cvt_pk_bf16_f32 v165, v170, v171
	v_cvt_pk_bf16_f32 v166, v172, v173
	v_cvt_pk_bf16_f32 v167, v174, v175
	v_mfma_f32_32x32x16_bf16 v[32:47], v[220:223], v[148:151], v[32:47]
	s_nop 1
	v_mfma_f32_32x32x16_bf16 v[112:127], v[184:187], v[160:163], v[112:127]
	s_xor_b32 s8, s27, 1
	s_mulk_i32 s8, 0x4800
	s_waitcnt vmcnt(0)
	v_mfma_f32_32x32x16_bf16 v[80:95], v[188:191], v[160:163], v[80:95]
	v_add_u32_e32 v15, s8, v2
	ds_write_b16 v15, v176 offset:34816
	v_mfma_f32_32x32x16_bf16 v[48:63], v[192:195], v[160:163], v[48:63]
	ds_write_b16_d16_hi v15, v176 offset:34960
	ds_write_b16 v15, v177 offset:35104
	ds_write_b16_d16_hi v15, v177 offset:35248
	v_mfma_f32_32x32x16_bf16 v[16:31], v[196:199], v[160:163], v[16:31]
	ds_write_b16 v15, v178 offset:35392
	ds_write_b16_d16_hi v15, v178 offset:35536
	v_mfma_f32_32x32x16_bf16 v[112:127], v[200:203], v[164:167], v[112:127]
	ds_write_b16 v15, v179 offset:35680
	ds_write_b16_d16_hi v15, v179 offset:35824
	ds_write_b16 v15, v180 offset:44032
	v_mfma_f32_32x32x16_bf16 v[80:95], v[212:215], v[164:167], v[80:95]
	ds_write_b16_d16_hi v15, v180 offset:44176
	ds_write_b16 v15, v181 offset:44320
	v_mfma_f32_32x32x16_bf16 v[48:63], v[216:219], v[164:167], v[48:63]
	ds_write_b16_d16_hi v15, v181 offset:44464
	ds_write_b16 v15, v182 offset:44608
	ds_write_b16_d16_hi v15, v182 offset:44752
	v_mfma_f32_32x32x16_bf16 v[16:31], v[220:223], v[164:167], v[16:31]
	ds_write_b16 v15, v183 offset:44896
	ds_write_b16_d16_hi v15, v183 offset:45040
	s_add_i32 s23, s23, 64
	s_cmpk_lg_i32 s23, 0x1100
	s_waitcnt vmcnt(0) lgkmcnt(0)
	s_barrier
	s_cbranch_scc0 .Lat_exit
	s_mov_b32 s26, s25
	s_branch .LBB0_439
